# speedup vs baseline: 1.0274x; 1.0274x over previous
.Lepi_tail:
	v_sub_u32_e32 v99, v55, v99
	v_cvt_f32_i32_e32 v99, v99
	v_max_f32_e32 v108, 0, v59
	v_max_f32_e32 v109, 0, v60
	v_fma_f32 v100, -v99, v108, v100
	v_fma_f32 v101, -v99, v109, v101
	ds_bpermute_b32 v2, v102, v100
	ds_bpermute_b32 v3, v102, v101
	v_mov_b32_e32 v4, 0x21e00
	v_lshl_add_u32 v4, v56, 2, v4
	s_waitcnt lgkmcnt(0)
	v_add_f32_e32 v100, v100, v2
	v_add_f32_e32 v101, v101, v3
	ds_bpermute_b32 v2, v1, v100
	ds_bpermute_b32 v3, v1, v101
	s_waitcnt lgkmcnt(0)
	v_add_f32_e32 v100, v100, v2
	v_add_f32_e32 v101, v101, v3
	s_and_saveexec_b64 s[0:1], s[66:67]
	ds_add_f32 v4, v100
	ds_add_f32 v4, v101 offset:64
